# recheck candidate extraction rewritten: per-tile 16-bit hit mask via v_cmp+v_addc, one aggregated extraction loop instead of 64 exec-masked blocks
# speedup vs baseline: 1.0265x; 1.0265x over previous
.LBB0_116:
	s_or_b64 exec, exec, s[0:1]
	v_or_b32_e32 v66, s25, v181
	v_cmp_lt_u32_e32 vcc, v66, v183
	v_mov_b32_e32 v67, 0
	v_mov_b32_e32 v186, 0
	v_mov_b32_e32 v187, 0
	s_waitcnt lgkmcnt(0)
	s_barrier
	s_and_saveexec_b64 s[0:1], vcc
	s_cbranch_execz .LBB0_118
	v_lshl_add_u32 v67, v66, 2, v249
	ds_read_b32 v67, v67
	s_waitcnt lgkmcnt(0)
	v_mul_lo_u32 v67, v67, s3
.LBB0_118:
	s_or_b64 exec, exec, s[0:1]
	v_add_u32_e32 v67, v182, v67
	ds_read_b128 v[162:165], v67
	ds_read_b128 v[94:97], v67 offset:32
	ds_read_b128 v[90:93], v67 offset:64
	ds_read_b128 v[86:89], v67 offset:96
	v_mov_b32_e32 v168, 0xff61b1e6
	s_and_saveexec_b64 s[0:1], vcc
	v_lshl_add_u32 v66, v66, 2, v250
	ds_read_b32 v168, v66
	s_or_b64 exec, exec, s[0:1]
	s_waitcnt lgkmcnt(3)
	v_mfma_f32_32x32x16_f16 v[66:81], v[98:101], v[162:165], v[2:17]
	s_waitcnt lgkmcnt(2)
	v_mfma_f32_32x32x16_f16 v[66:81], v[102:105], v[94:97], v[66:81]
	s_waitcnt lgkmcnt(1)
	v_mfma_f32_32x32x16_f16 v[66:81], v[106:109], v[90:93], v[66:81]
	s_waitcnt lgkmcnt(0)
	v_mfma_f32_32x32x16_f16 v[66:81], v[110:113], v[86:89], v[66:81]
	s_nop 11
	v_min3_f32 v254, v66, v67, v68
	v_min3_f32 v254, v254, v69, v70
	v_min3_f32 v254, v254, v71, v72
	v_min3_f32 v254, v254, v73, v74
	v_min3_f32 v254, v254, v75, v76
	v_min3_f32 v254, v254, v77, v78
	v_min3_f32 v254, v254, v79, v80
	v_min_f32_e32 v254, v254, v81
	v_cmp_lt_f32_e32 vcc, v254, v168
	s_cbranch_vccz .Lrc_skip_tile0
	v_mov_b32_e32 v254, 0
	v_cmp_lt_f32_e64 s[0:1], v81, v168
	v_cmp_lt_f32_e64 s[14:15], v80, v168
	v_cmp_lt_f32_e64 s[16:17], v79, v168
	v_addc_co_u32_e64 v254, vcc, v254, v254, s[0:1]
	v_cmp_lt_f32_e64 s[0:1], v78, v168
	v_addc_co_u32_e64 v254, vcc, v254, v254, s[14:15]
	v_cmp_lt_f32_e64 s[14:15], v77, v168
	v_addc_co_u32_e64 v254, vcc, v254, v254, s[16:17]
	v_cmp_lt_f32_e64 s[16:17], v76, v168
	v_addc_co_u32_e64 v254, vcc, v254, v254, s[0:1]
	v_cmp_lt_f32_e64 s[0:1], v75, v168
	v_addc_co_u32_e64 v254, vcc, v254, v254, s[14:15]
	v_cmp_lt_f32_e64 s[14:15], v74, v168
	v_addc_co_u32_e64 v254, vcc, v254, v254, s[16:17]
	v_cmp_lt_f32_e64 s[16:17], v73, v168
	v_addc_co_u32_e64 v254, vcc, v254, v254, s[0:1]
	v_cmp_lt_f32_e64 s[0:1], v72, v168
	v_addc_co_u32_e64 v254, vcc, v254, v254, s[14:15]
	v_cmp_lt_f32_e64 s[14:15], v71, v168
	v_addc_co_u32_e64 v254, vcc, v254, v254, s[16:17]
	v_cmp_lt_f32_e64 s[16:17], v70, v168
	v_addc_co_u32_e64 v254, vcc, v254, v254, s[0:1]
	v_cmp_lt_f32_e64 s[0:1], v69, v168
	v_addc_co_u32_e64 v254, vcc, v254, v254, s[14:15]
	v_cmp_lt_f32_e64 s[14:15], v68, v168
	v_addc_co_u32_e64 v254, vcc, v254, v254, s[16:17]
	v_cmp_lt_f32_e64 s[16:17], v67, v168
	v_addc_co_u32_e64 v254, vcc, v254, v254, s[0:1]
	v_cmp_lt_f32_e64 s[0:1], v66, v168
	v_addc_co_u32_e64 v254, vcc, v254, v254, s[14:15]
	v_addc_co_u32_e64 v254, vcc, v254, v254, s[16:17]
	v_addc_co_u32_e64 v254, vcc, v254, v254, s[0:1]
	v_or_b32_e32 v186, v186, v254
.Lrc_skip_tile0:
	v_mfma_f32_32x32x16_f16 v[66:81], v[114:117], v[162:165], v[18:33]
	v_mfma_f32_32x32x16_f16 v[66:81], v[118:121], v[94:97], v[66:81]
	v_mfma_f32_32x32x16_f16 v[66:81], v[122:125], v[90:93], v[66:81]
	v_mfma_f32_32x32x16_f16 v[66:81], v[126:129], v[86:89], v[66:81]
	s_nop 11
	v_min3_f32 v254, v66, v67, v68
	v_min3_f32 v254, v254, v69, v70
	v_min3_f32 v254, v254, v71, v72
	v_min3_f32 v254, v254, v73, v74
	v_min3_f32 v254, v254, v75, v76
	v_min3_f32 v254, v254, v77, v78
	v_min3_f32 v254, v254, v79, v80
	v_min_f32_e32 v254, v254, v81
	v_cmp_lt_f32_e32 vcc, v254, v168
	s_cbranch_vccz .Lrc_skip_tile1
	v_mov_b32_e32 v254, 0
	v_cmp_lt_f32_e64 s[0:1], v81, v168
	v_cmp_lt_f32_e64 s[14:15], v80, v168
	v_cmp_lt_f32_e64 s[16:17], v79, v168
	v_addc_co_u32_e64 v254, vcc, v254, v254, s[0:1]
	v_cmp_lt_f32_e64 s[0:1], v78, v168
	v_addc_co_u32_e64 v254, vcc, v254, v254, s[14:15]
	v_cmp_lt_f32_e64 s[14:15], v77, v168
	v_addc_co_u32_e64 v254, vcc, v254, v254, s[16:17]
	v_cmp_lt_f32_e64 s[16:17], v76, v168
	v_addc_co_u32_e64 v254, vcc, v254, v254, s[0:1]
	v_cmp_lt_f32_e64 s[0:1], v75, v168
	v_addc_co_u32_e64 v254, vcc, v254, v254, s[14:15]
	v_cmp_lt_f32_e64 s[14:15], v74, v168
	v_addc_co_u32_e64 v254, vcc, v254, v254, s[16:17]
	v_cmp_lt_f32_e64 s[16:17], v73, v168
	v_addc_co_u32_e64 v254, vcc, v254, v254, s[0:1]
	v_cmp_lt_f32_e64 s[0:1], v72, v168
	v_addc_co_u32_e64 v254, vcc, v254, v254, s[14:15]
	v_cmp_lt_f32_e64 s[14:15], v71, v168
	v_addc_co_u32_e64 v254, vcc, v254, v254, s[16:17]
	v_cmp_lt_f32_e64 s[16:17], v70, v168
	v_addc_co_u32_e64 v254, vcc, v254, v254, s[0:1]
	v_cmp_lt_f32_e64 s[0:1], v69, v168
	v_addc_co_u32_e64 v254, vcc, v254, v254, s[14:15]
	v_cmp_lt_f32_e64 s[14:15], v68, v168
	v_addc_co_u32_e64 v254, vcc, v254, v254, s[16:17]
	v_cmp_lt_f32_e64 s[16:17], v67, v168
	v_addc_co_u32_e64 v254, vcc, v254, v254, s[0:1]
	v_cmp_lt_f32_e64 s[0:1], v66, v168
	v_addc_co_u32_e64 v254, vcc, v254, v254, s[14:15]
	v_addc_co_u32_e64 v254, vcc, v254, v254, s[16:17]
	v_addc_co_u32_e64 v254, vcc, v254, v254, s[0:1]
	v_lshl_or_b32 v186, v254, 16, v186
.Lrc_skip_tile1:
	v_mfma_f32_32x32x16_f16 v[66:81], v[130:133], v[162:165], v[34:49]
	v_mfma_f32_32x32x16_f16 v[66:81], v[134:137], v[94:97], v[66:81]
	v_mfma_f32_32x32x16_f16 v[66:81], v[138:141], v[90:93], v[66:81]
	v_mfma_f32_32x32x16_f16 v[66:81], v[142:145], v[86:89], v[66:81]
	s_nop 11
	v_min3_f32 v254, v66, v67, v68
	v_min3_f32 v254, v254, v69, v70
	v_min3_f32 v254, v254, v71, v72
	v_min3_f32 v254, v254, v73, v74
	v_min3_f32 v254, v254, v75, v76
	v_min3_f32 v254, v254, v77, v78
	v_min3_f32 v254, v254, v79, v80
	v_min_f32_e32 v254, v254, v81
	v_cmp_lt_f32_e32 vcc, v254, v168
	s_cbranch_vccz .Lrc_skip_tile2
	v_mov_b32_e32 v254, 0
	v_cmp_lt_f32_e64 s[0:1], v81, v168
	v_cmp_lt_f32_e64 s[14:15], v80, v168
	v_cmp_lt_f32_e64 s[16:17], v79, v168
	v_addc_co_u32_e64 v254, vcc, v254, v254, s[0:1]
	v_cmp_lt_f32_e64 s[0:1], v78, v168
	v_addc_co_u32_e64 v254, vcc, v254, v254, s[14:15]
	v_cmp_lt_f32_e64 s[14:15], v77, v168
	v_addc_co_u32_e64 v254, vcc, v254, v254, s[16:17]
	v_cmp_lt_f32_e64 s[16:17], v76, v168
	v_addc_co_u32_e64 v254, vcc, v254, v254, s[0:1]
	v_cmp_lt_f32_e64 s[0:1], v75, v168
	v_addc_co_u32_e64 v254, vcc, v254, v254, s[14:15]
	v_cmp_lt_f32_e64 s[14:15], v74, v168
	v_addc_co_u32_e64 v254, vcc, v254, v254, s[16:17]
	v_cmp_lt_f32_e64 s[16:17], v73, v168
	v_addc_co_u32_e64 v254, vcc, v254, v254, s[0:1]
	v_cmp_lt_f32_e64 s[0:1], v72, v168
	v_addc_co_u32_e64 v254, vcc, v254, v254, s[14:15]
	v_cmp_lt_f32_e64 s[14:15], v71, v168
	v_addc_co_u32_e64 v254, vcc, v254, v254, s[16:17]
	v_cmp_lt_f32_e64 s[16:17], v70, v168
	v_addc_co_u32_e64 v254, vcc, v254, v254, s[0:1]
	v_cmp_lt_f32_e64 s[0:1], v69, v168
	v_addc_co_u32_e64 v254, vcc, v254, v254, s[14:15]
	v_cmp_lt_f32_e64 s[14:15], v68, v168
	v_addc_co_u32_e64 v254, vcc, v254, v254, s[16:17]
	v_cmp_lt_f32_e64 s[16:17], v67, v168
	v_addc_co_u32_e64 v254, vcc, v254, v254, s[0:1]
	v_cmp_lt_f32_e64 s[0:1], v66, v168
	v_addc_co_u32_e64 v254, vcc, v254, v254, s[14:15]
	v_addc_co_u32_e64 v254, vcc, v254, v254, s[16:17]
	v_addc_co_u32_e64 v254, vcc, v254, v254, s[0:1]
	v_or_b32_e32 v187, v187, v254
.Lrc_skip_tile2:
	v_mfma_f32_32x32x16_f16 v[66:81], v[146:149], v[162:165], v[50:65]
	v_mfma_f32_32x32x16_f16 v[66:81], v[150:153], v[94:97], v[66:81]
	v_mfma_f32_32x32x16_f16 v[66:81], v[154:157], v[90:93], v[66:81]
	v_mfma_f32_32x32x16_f16 v[66:81], v[158:161], v[86:89], v[66:81]
	s_nop 11
	v_min3_f32 v254, v66, v67, v68
	v_min3_f32 v254, v254, v69, v70
	v_min3_f32 v254, v254, v71, v72
	v_min3_f32 v254, v254, v73, v74
	v_min3_f32 v254, v254, v75, v76
	v_min3_f32 v254, v254, v77, v78
	v_min3_f32 v254, v254, v79, v80
	v_min_f32_e32 v254, v254, v81
	v_cmp_lt_f32_e32 vcc, v254, v168
	s_cbranch_vccz .Lrc_skip_tile3
	v_mov_b32_e32 v254, 0
	v_cmp_lt_f32_e64 s[0:1], v81, v168
	v_cmp_lt_f32_e64 s[14:15], v80, v168
	v_cmp_lt_f32_e64 s[16:17], v79, v168
	v_addc_co_u32_e64 v254, vcc, v254, v254, s[0:1]
	v_cmp_lt_f32_e64 s[0:1], v78, v168
	v_addc_co_u32_e64 v254, vcc, v254, v254, s[14:15]
	v_cmp_lt_f32_e64 s[14:15], v77, v168
	v_addc_co_u32_e64 v254, vcc, v254, v254, s[16:17]
	v_cmp_lt_f32_e64 s[16:17], v76, v168
	v_addc_co_u32_e64 v254, vcc, v254, v254, s[0:1]
	v_cmp_lt_f32_e64 s[0:1], v75, v168
	v_addc_co_u32_e64 v254, vcc, v254, v254, s[14:15]
	v_cmp_lt_f32_e64 s[14:15], v74, v168
	v_addc_co_u32_e64 v254, vcc, v254, v254, s[16:17]
	v_cmp_lt_f32_e64 s[16:17], v73, v168
	v_addc_co_u32_e64 v254, vcc, v254, v254, s[0:1]
	v_cmp_lt_f32_e64 s[0:1], v72, v168
	v_addc_co_u32_e64 v254, vcc, v254, v254, s[14:15]
	v_cmp_lt_f32_e64 s[14:15], v71, v168
	v_addc_co_u32_e64 v254, vcc, v254, v254, s[16:17]
	v_cmp_lt_f32_e64 s[16:17], v70, v168
	v_addc_co_u32_e64 v254, vcc, v254, v254, s[0:1]
	v_cmp_lt_f32_e64 s[0:1], v69, v168
	v_addc_co_u32_e64 v254, vcc, v254, v254, s[14:15]
	v_cmp_lt_f32_e64 s[14:15], v68, v168
	v_addc_co_u32_e64 v254, vcc, v254, v254, s[16:17]
	v_cmp_lt_f32_e64 s[16:17], v67, v168
	v_addc_co_u32_e64 v254, vcc, v254, v254, s[0:1]
	v_cmp_lt_f32_e64 s[0:1], v66, v168
	v_addc_co_u32_e64 v254, vcc, v254, v254, s[14:15]
	v_addc_co_u32_e64 v254, vcc, v254, v254, s[16:17]
	v_addc_co_u32_e64 v254, vcc, v254, v254, s[0:1]
	v_lshl_or_b32 v187, v254, 16, v187
.Lrc_skip_tile3:
.Lcx_loopa:
	v_cmp_ne_u32_e32 vcc, 0, v186
	s_cbranch_vccz .Lcx_donea
	s_and_saveexec_b64 s[0:1], vcc
	v_ffbl_b32_e32 v188, v186
	v_lshlrev_b32_e64 v189, v188, 1
	v_xor_b32_e32 v186, v186, v189
	v_lshrrev_b32_e32 v189, 2, v188
	v_and_b32_e32 v188, 3, v188
	v_lshl_or_b32 v189, v189, 3, v188
	v_or3_b32 v189, v189, v179, 0
	s_mov_b64 s[16:17], exec
	v_mbcnt_lo_u32_b32 v190, s16, 0
	v_mbcnt_hi_u32_b32 v190, s17, v190
	v_cmp_eq_u32_e32 vcc, 0, v190
	s_and_saveexec_b64 s[14:15], vcc
	s_bcnt1_i32_b64 s16, s[16:17]
	v_mov_b32_e32 v191, s16
	ds_add_rtn_u32 v191, v248, v191
	s_or_b64 exec, exec, s[14:15]
	s_waitcnt lgkmcnt(0)
	v_readfirstlane_b32 s14, v191
	s_nop 1
	v_add_u32_e32 v190, s14, v190
	v_cmp_gt_u32_e32 vcc, s20, v190
	s_and_b64 exec, exec, vcc
	v_lshl_add_u32 v190, v190, 2, v246
	ds_write_b32 v190, v189
	s_or_b64 exec, exec, s[0:1]
	s_branch .Lcx_loopa
.Lcx_donea:
.Lcx_loopb:
	v_cmp_ne_u32_e32 vcc, 0, v187
	s_cbranch_vccz .Lcx_doneb
	s_and_saveexec_b64 s[0:1], vcc
	v_ffbl_b32_e32 v188, v187
	v_lshlrev_b32_e64 v189, v188, 1
	v_xor_b32_e32 v187, v187, v189
	v_lshrrev_b32_e32 v189, 2, v188
	v_and_b32_e32 v188, 3, v188
	v_lshl_or_b32 v189, v189, 3, v188
	v_or3_b32 v189, v189, v179, 64
	s_mov_b64 s[16:17], exec
	v_mbcnt_lo_u32_b32 v190, s16, 0
	v_mbcnt_hi_u32_b32 v190, s17, v190
	v_cmp_eq_u32_e32 vcc, 0, v190
	s_and_saveexec_b64 s[14:15], vcc
	s_bcnt1_i32_b64 s16, s[16:17]
	v_mov_b32_e32 v191, s16
	ds_add_rtn_u32 v191, v248, v191
	s_or_b64 exec, exec, s[14:15]
	s_waitcnt lgkmcnt(0)
	v_readfirstlane_b32 s14, v191
	s_nop 1
	v_add_u32_e32 v190, s14, v190
	v_cmp_gt_u32_e32 vcc, s20, v190
	s_and_b64 exec, exec, vcc
	v_lshl_add_u32 v190, v190, 2, v246
	ds_write_b32 v190, v189
	s_or_b64 exec, exec, s[0:1]
	s_branch .Lcx_loopb
